# P4 (FFN gate/up, int8) epilogue rewritten by hand with packed f32 mul/fma and 32-bit store offsets; same arithmetic order
# baseline (speedup 1.0000x reference)
.LBB0_759:
	s_lshl_b32 s15, s57, 11
	v_mov_b32_e32 v196, v198
	s_and_b32 s15, s15, 0x800
	s_add_i32 s15, s52, s15
	v_and_b32_e32 v210, 15, v196
	v_lshl_add_u32 v211, v210, 3, s15
	ds_read2_b64 v[192:195], v211 offset1:16
	v_ashrrev_i32_e32 v214, 1, v196
	s_lshl_b32 s15, s22, 8
	s_add_i32 s15, s15, s50
	v_or_b32_e32 v210, s15, v210
	s_waitcnt lgkmcnt(0)
	v_mov_b32_e32 v196, v193
	v_lshlrev_b64 v[212:213], s54, v[196:197]
	v_min_u32_e32 v193, 1, v212
	v_or_b32_e32 v193, v213, v193
	v_cvt_f32_u32_e32 v193, v193
	v_cvt_f32_u32_e32 v192, v192
	s_sub_i32 s15, 32, s54
	v_mov_b32_e32 v196, v195
	v_ldexp_f32 v193, v193, s15
	v_fmamk_f32 v212, v192, 0x2e000000, v209
	v_fmac_f32_e32 v212, 0x3e000000, v193
	v_lshlrev_b64 v[192:193], s54, v[196:197]
	v_min_u32_e32 v192, 1, v192
	v_or_b32_e32 v192, v193, v192
	v_cvt_f32_u32_e32 v196, v192
	v_cvt_f32_u32_e32 v213, v194
	ds_read2_b64 v[192:195], v211 offset0:32 offset1:48
	v_rsq_f32_e32 v215, v212
	v_ldexp_f32 v196, v196, s15
	v_fmamk_f32 v212, v213, 0x2e000000, v209
	v_fmac_f32_e32 v212, 0x3e000000, v196
	s_waitcnt lgkmcnt(0)
	v_mov_b32_e32 v196, v193
	v_rsq_f32_e32 v216, v212
	v_lshlrev_b64 v[212:213], s54, v[196:197]
	v_min_u32_e32 v193, 1, v212
	v_or_b32_e32 v193, v213, v193
	v_cvt_f32_u32_e32 v193, v193
	v_cvt_f32_u32_e32 v192, v192
	v_mov_b32_e32 v196, v195
	v_cvt_f32_u32_e32 v213, v194
	v_ldexp_f32 v193, v193, s15
	v_fmamk_f32 v212, v192, 0x2e000000, v209
	v_fmac_f32_e32 v212, 0x3e000000, v193
	v_lshlrev_b64 v[192:193], s54, v[196:197]
	v_min_u32_e32 v192, 1, v192
	v_or_b32_e32 v192, v193, v192
	v_cvt_f32_u32_e32 v196, v192
	ds_read2_b64 v[192:195], v211 offset0:128 offset1:144
	v_rsq_f32_e32 v217, v212
	v_fmamk_f32 v212, v213, 0x2e000000, v209
	v_ldexp_f32 v196, v196, s15
	v_fmac_f32_e32 v212, 0x3e000000, v196
	s_waitcnt lgkmcnt(0)
	v_mov_b32_e32 v196, v193
	v_rsq_f32_e32 v218, v212
	v_lshlrev_b64 v[212:213], s54, v[196:197]
	v_min_u32_e32 v193, 1, v212
	v_or_b32_e32 v193, v213, v193
	v_cvt_f32_u32_e32 v193, v193
	v_cvt_f32_u32_e32 v192, v192
	v_mov_b32_e32 v196, v195
	v_cvt_f32_u32_e32 v219, v194
	v_ldexp_f32 v212, v193, s15
	v_fmamk_f32 v213, v192, 0x2e000000, v209
	v_lshlrev_b64 v[192:193], s54, v[196:197]
	v_min_u32_e32 v192, 1, v192
	v_or_b32_e32 v192, v193, v192
	v_cvt_f32_u32_e32 v196, v192
	ds_read2_b64 v[192:195], v211 offset0:160 offset1:176
	v_fmac_f32_e32 v213, 0x3e000000, v212
	v_rsq_f32_e32 v211, v213
	v_ldexp_f32 v220, v196, s15
	v_fmamk_f32 v219, v219, 0x2e000000, v209
	s_waitcnt lgkmcnt(0)
	v_mov_b32_e32 v196, v193
	v_lshlrev_b64 v[212:213], s54, v[196:197]
	v_min_u32_e32 v193, 1, v212
	v_or_b32_e32 v193, v213, v193
	v_cvt_f32_u32_e32 v193, v193
	v_cvt_f32_u32_e32 v192, v192
	v_fmac_f32_e32 v219, 0x3e000000, v220
	v_mov_b32_e32 v196, v195
	v_rsq_f32_e32 v212, v219
	v_ldexp_f32 v213, v193, s15
	v_fmamk_f32 v219, v192, 0x2e000000, v209
	v_lshlrev_b64 v[192:193], s54, v[196:197]
	v_min_u32_e32 v192, 1, v192
	v_or_b32_e32 v192, v193, v192
	v_cvt_f32_u32_e32 v192, v192
	v_cvt_f32_u32_e32 v193, v194
	v_fmac_f32_e32 v219, 0x3e000000, v213
	v_rsq_f32_e32 v194, v219
	v_ldexp_f32 v192, v192, s15
	v_fmamk_f32 v193, v193, 0x2e000000, v209
	v_fmac_f32_e32 v193, 0x3e000000, v192
	v_rsq_f32_e32 v192, v193
	v_mul_f32_e32 v224, 0x37d834f1, v215
	v_mul_f32_e32 v225, 0x37d834f1, v216
	v_mul_f32_e32 v226, 0x37d834f1, v217
	v_mul_f32_e32 v227, 0x37d834f1, v218
	v_mul_f32_e32 v228, 0x37d834f1, v211
	v_mul_f32_e32 v229, 0x37d834f1, v212
	v_mul_f32_e32 v230, 0x37d834f1, v194
	v_mul_f32_e32 v231, 0x37d834f1, v192
	s_lshl_b32 s15, s56, 7
	v_and_b32_e32 v214, -8, v214
	s_or_b32 s15, s15, s51
	v_add_u32_e32 v214, s15, v214
	v_lshlrev_b32_e32 v214, 1, v214
	v_mad_u32_u24 v232, v210, s53, v214
	v_mul_f32_e32 v78, 0xbfb8aa3b, v224
	v_mul_f32_e32 v20, v224, v224
	v_rcp_f32_e32 v20, v20
	v_cvt_f32_i32_e32 v184, v184
	v_cvt_f32_i32_e32 v185, v185
	v_cvt_f32_i32_e32 v186, v186
	v_cvt_f32_i32_e32 v187, v187
	v_cvt_f32_i32_e32 v176, v176
	v_cvt_f32_i32_e32 v177, v177
	v_cvt_f32_i32_e32 v178, v178
	v_cvt_f32_i32_e32 v179, v179
	v_cvt_f32_i32_e32 v188, v188
	v_cvt_f32_i32_e32 v189, v189
	v_cvt_f32_i32_e32 v190, v190
	v_cvt_f32_i32_e32 v191, v191
	v_cvt_f32_i32_e32 v180, v180
	v_cvt_f32_i32_e32 v181, v181
	v_cvt_f32_i32_e32 v182, v182
	v_cvt_f32_i32_e32 v183, v183
	v_pk_mul_f32 v[64:65], v[184:185], v[78:79] op_sel_hi:[1,0]
	v_pk_mul_f32 v[66:67], v[186:187], v[78:79] op_sel_hi:[1,0]
	v_pk_mul_f32 v[68:69], v[176:177], v[78:79] op_sel_hi:[1,0]
	v_pk_mul_f32 v[70:71], v[178:179], v[78:79] op_sel_hi:[1,0]
	v_exp_f32_e32 v64, v64
	v_exp_f32_e32 v65, v65
	v_exp_f32_e32 v66, v66
	v_exp_f32_e32 v67, v67
	v_exp_f32_e32 v68, v68
	v_exp_f32_e32 v69, v69
	v_exp_f32_e32 v70, v70
	v_exp_f32_e32 v71, v71
	v_pk_mul_f32 v[184:185], v[188:189], v[184:185]
	v_pk_mul_f32 v[186:187], v[190:191], v[186:187]
	v_pk_mul_f32 v[176:177], v[180:181], v[176:177]
	v_pk_mul_f32 v[178:179], v[182:183], v[178:179]
	v_pk_fma_f32 v[64:65], v[64:65], v[20:21], v[20:21] op_sel_hi:[1,0,0]
	v_pk_fma_f32 v[66:67], v[66:67], v[20:21], v[20:21] op_sel_hi:[1,0,0]
	v_pk_fma_f32 v[68:69], v[68:69], v[20:21], v[20:21] op_sel_hi:[1,0,0]
	v_pk_fma_f32 v[70:71], v[70:71], v[20:21], v[20:21] op_sel_hi:[1,0,0]
	v_rcp_f32_e32 v64, v64
	v_rcp_f32_e32 v65, v65
	v_rcp_f32_e32 v66, v66
	v_rcp_f32_e32 v67, v67
	v_rcp_f32_e32 v68, v68
	v_rcp_f32_e32 v69, v69
	v_rcp_f32_e32 v70, v70
	v_rcp_f32_e32 v71, v71
	v_mov_b32_e32 v76, v232
	v_pk_mul_f32 v[184:185], v[184:185], v[64:65]
	v_pk_mul_f32 v[186:187], v[186:187], v[66:67]
	v_pk_mul_f32 v[176:177], v[176:177], v[68:69]
	v_pk_mul_f32 v[178:179], v[178:179], v[70:71]
	v_cvt_pk_bf16_f32 v72, v184, v185
	v_cvt_pk_bf16_f32 v73, v186, v187
	v_cvt_pk_bf16_f32 v74, v176, v177
	v_cvt_pk_bf16_f32 v75, v178, v179
	global_store_dwordx4 v76, v[72:75], s[8:9]
	v_mul_f32_e32 v94, 0xbfb8aa3b, v225
	v_mul_f32_e32 v24, v225, v225
	v_rcp_f32_e32 v24, v24
	v_cvt_f32_i32_e32 v168, v168
	v_cvt_f32_i32_e32 v169, v169
	v_cvt_f32_i32_e32 v170, v170
	v_cvt_f32_i32_e32 v171, v171
	v_cvt_f32_i32_e32 v160, v160
	v_cvt_f32_i32_e32 v161, v161
	v_cvt_f32_i32_e32 v162, v162
	v_cvt_f32_i32_e32 v163, v163
	v_cvt_f32_i32_e32 v172, v172
	v_cvt_f32_i32_e32 v173, v173
	v_cvt_f32_i32_e32 v174, v174
	v_cvt_f32_i32_e32 v175, v175
	v_cvt_f32_i32_e32 v164, v164
	v_cvt_f32_i32_e32 v165, v165
	v_cvt_f32_i32_e32 v166, v166
	v_cvt_f32_i32_e32 v167, v167
	v_pk_mul_f32 v[80:81], v[168:169], v[94:95] op_sel_hi:[1,0]
	v_pk_mul_f32 v[82:83], v[170:171], v[94:95] op_sel_hi:[1,0]
	v_pk_mul_f32 v[84:85], v[160:161], v[94:95] op_sel_hi:[1,0]
	v_pk_mul_f32 v[86:87], v[162:163], v[94:95] op_sel_hi:[1,0]
	v_exp_f32_e32 v80, v80
	v_exp_f32_e32 v81, v81
	v_exp_f32_e32 v82, v82
	v_exp_f32_e32 v83, v83
	v_exp_f32_e32 v84, v84
	v_exp_f32_e32 v85, v85
	v_exp_f32_e32 v86, v86
	v_exp_f32_e32 v87, v87
	v_pk_mul_f32 v[168:169], v[172:173], v[168:169]
	v_pk_mul_f32 v[170:171], v[174:175], v[170:171]
	v_pk_mul_f32 v[160:161], v[164:165], v[160:161]
	v_pk_mul_f32 v[162:163], v[166:167], v[162:163]
	v_pk_fma_f32 v[80:81], v[80:81], v[24:25], v[24:25] op_sel_hi:[1,0,0]
	v_pk_fma_f32 v[82:83], v[82:83], v[24:25], v[24:25] op_sel_hi:[1,0,0]
	v_pk_fma_f32 v[84:85], v[84:85], v[24:25], v[24:25] op_sel_hi:[1,0,0]
	v_pk_fma_f32 v[86:87], v[86:87], v[24:25], v[24:25] op_sel_hi:[1,0,0]
	v_rcp_f32_e32 v80, v80
	v_rcp_f32_e32 v81, v81
	v_rcp_f32_e32 v82, v82
	v_rcp_f32_e32 v83, v83
	v_rcp_f32_e32 v84, v84
	v_rcp_f32_e32 v85, v85
	v_rcp_f32_e32 v86, v86
	v_rcp_f32_e32 v87, v87
	v_add_u32_e32 v92, 0x2c000, v232
	v_pk_mul_f32 v[168:169], v[168:169], v[80:81]
	v_pk_mul_f32 v[170:171], v[170:171], v[82:83]
	v_pk_mul_f32 v[160:161], v[160:161], v[84:85]
	v_pk_mul_f32 v[162:163], v[162:163], v[86:87]
	v_cvt_pk_bf16_f32 v88, v168, v169
	v_cvt_pk_bf16_f32 v89, v170, v171
	v_cvt_pk_bf16_f32 v90, v160, v161
	v_cvt_pk_bf16_f32 v91, v162, v163
	global_store_dwordx4 v92, v[88:91], s[8:9]
	v_mul_f32_e32 v78, 0xbfb8aa3b, v226
	v_mul_f32_e32 v20, v226, v226
	v_rcp_f32_e32 v20, v20
	v_cvt_f32_i32_e32 v152, v152
	v_cvt_f32_i32_e32 v153, v153
	v_cvt_f32_i32_e32 v154, v154
	v_cvt_f32_i32_e32 v155, v155
	v_cvt_f32_i32_e32 v144, v144
	v_cvt_f32_i32_e32 v145, v145
	v_cvt_f32_i32_e32 v146, v146
	v_cvt_f32_i32_e32 v147, v147
	v_cvt_f32_i32_e32 v156, v156
	v_cvt_f32_i32_e32 v157, v157
	v_cvt_f32_i32_e32 v158, v158
	v_cvt_f32_i32_e32 v159, v159
	v_cvt_f32_i32_e32 v148, v148
	v_cvt_f32_i32_e32 v149, v149
	v_cvt_f32_i32_e32 v150, v150
	v_cvt_f32_i32_e32 v151, v151
	v_pk_mul_f32 v[64:65], v[152:153], v[78:79] op_sel_hi:[1,0]
	v_pk_mul_f32 v[66:67], v[154:155], v[78:79] op_sel_hi:[1,0]
	v_pk_mul_f32 v[68:69], v[144:145], v[78:79] op_sel_hi:[1,0]
	v_pk_mul_f32 v[70:71], v[146:147], v[78:79] op_sel_hi:[1,0]
	v_exp_f32_e32 v64, v64
	v_exp_f32_e32 v65, v65
	v_exp_f32_e32 v66, v66
	v_exp_f32_e32 v67, v67
	v_exp_f32_e32 v68, v68
	v_exp_f32_e32 v69, v69
	v_exp_f32_e32 v70, v70
	v_exp_f32_e32 v71, v71
	v_pk_mul_f32 v[152:153], v[156:157], v[152:153]
	v_pk_mul_f32 v[154:155], v[158:159], v[154:155]
	v_pk_mul_f32 v[144:145], v[148:149], v[144:145]
	v_pk_mul_f32 v[146:147], v[150:151], v[146:147]
	v_pk_fma_f32 v[64:65], v[64:65], v[20:21], v[20:21] op_sel_hi:[1,0,0]
	v_pk_fma_f32 v[66:67], v[66:67], v[20:21], v[20:21] op_sel_hi:[1,0,0]
	v_pk_fma_f32 v[68:69], v[68:69], v[20:21], v[20:21] op_sel_hi:[1,0,0]
	v_pk_fma_f32 v[70:71], v[70:71], v[20:21], v[20:21] op_sel_hi:[1,0,0]
	v_rcp_f32_e32 v64, v64
	v_rcp_f32_e32 v65, v65
	v_rcp_f32_e32 v66, v66
	v_rcp_f32_e32 v67, v67
	v_rcp_f32_e32 v68, v68
	v_rcp_f32_e32 v69, v69
	v_rcp_f32_e32 v70, v70
	v_rcp_f32_e32 v71, v71
	v_add_u32_e32 v76, 0x58000, v232
	v_pk_mul_f32 v[152:153], v[152:153], v[64:65]
	v_pk_mul_f32 v[154:155], v[154:155], v[66:67]
	v_pk_mul_f32 v[144:145], v[144:145], v[68:69]
	v_pk_mul_f32 v[146:147], v[146:147], v[70:71]
	v_cvt_pk_bf16_f32 v72, v152, v153
	v_cvt_pk_bf16_f32 v73, v154, v155
	v_cvt_pk_bf16_f32 v74, v144, v145
	v_cvt_pk_bf16_f32 v75, v146, v147
	global_store_dwordx4 v76, v[72:75], s[8:9]
	v_mul_f32_e32 v94, 0xbfb8aa3b, v227
	v_mul_f32_e32 v24, v227, v227
	v_rcp_f32_e32 v24, v24
	v_cvt_f32_i32_e32 v136, v136
	v_cvt_f32_i32_e32 v137, v137
	v_cvt_f32_i32_e32 v138, v138
	v_cvt_f32_i32_e32 v139, v139
	v_cvt_f32_i32_e32 v128, v128
	v_cvt_f32_i32_e32 v129, v129
	v_cvt_f32_i32_e32 v130, v130
	v_cvt_f32_i32_e32 v131, v131
	v_cvt_f32_i32_e32 v140, v140
	v_cvt_f32_i32_e32 v141, v141
	v_cvt_f32_i32_e32 v142, v142
	v_cvt_f32_i32_e32 v143, v143
	v_cvt_f32_i32_e32 v132, v132
	v_cvt_f32_i32_e32 v133, v133
	v_cvt_f32_i32_e32 v134, v134
	v_cvt_f32_i32_e32 v135, v135
	v_pk_mul_f32 v[80:81], v[136:137], v[94:95] op_sel_hi:[1,0]
	v_pk_mul_f32 v[82:83], v[138:139], v[94:95] op_sel_hi:[1,0]
	v_pk_mul_f32 v[84:85], v[128:129], v[94:95] op_sel_hi:[1,0]
	v_pk_mul_f32 v[86:87], v[130:131], v[94:95] op_sel_hi:[1,0]
	v_exp_f32_e32 v80, v80
	v_exp_f32_e32 v81, v81
	v_exp_f32_e32 v82, v82
	v_exp_f32_e32 v83, v83
	v_exp_f32_e32 v84, v84
	v_exp_f32_e32 v85, v85
	v_exp_f32_e32 v86, v86
	v_exp_f32_e32 v87, v87
	v_pk_mul_f32 v[136:137], v[140:141], v[136:137]
	v_pk_mul_f32 v[138:139], v[142:143], v[138:139]
	v_pk_mul_f32 v[128:129], v[132:133], v[128:129]
	v_pk_mul_f32 v[130:131], v[134:135], v[130:131]
	v_pk_fma_f32 v[80:81], v[80:81], v[24:25], v[24:25] op_sel_hi:[1,0,0]
	v_pk_fma_f32 v[82:83], v[82:83], v[24:25], v[24:25] op_sel_hi:[1,0,0]
	v_pk_fma_f32 v[84:85], v[84:85], v[24:25], v[24:25] op_sel_hi:[1,0,0]
	v_pk_fma_f32 v[86:87], v[86:87], v[24:25], v[24:25] op_sel_hi:[1,0,0]
	v_rcp_f32_e32 v80, v80
	v_rcp_f32_e32 v81, v81
	v_rcp_f32_e32 v82, v82
	v_rcp_f32_e32 v83, v83
	v_rcp_f32_e32 v84, v84
	v_rcp_f32_e32 v85, v85
	v_rcp_f32_e32 v86, v86
	v_rcp_f32_e32 v87, v87
	v_add_u32_e32 v92, 0x84000, v232
	v_pk_mul_f32 v[136:137], v[136:137], v[80:81]
	v_pk_mul_f32 v[138:139], v[138:139], v[82:83]
	v_pk_mul_f32 v[128:129], v[128:129], v[84:85]
	v_pk_mul_f32 v[130:131], v[130:131], v[86:87]
	v_cvt_pk_bf16_f32 v88, v136, v137
	v_cvt_pk_bf16_f32 v89, v138, v139
	v_cvt_pk_bf16_f32 v90, v128, v129
	v_cvt_pk_bf16_f32 v91, v130, v131
	global_store_dwordx4 v92, v[88:91], s[8:9]
	v_mul_f32_e32 v78, 0xbfb8aa3b, v228
	v_mul_f32_e32 v20, v228, v228
	v_rcp_f32_e32 v20, v20
	v_cvt_f32_i32_e32 v120, v120
	v_cvt_f32_i32_e32 v121, v121
	v_cvt_f32_i32_e32 v122, v122
	v_cvt_f32_i32_e32 v123, v123
	v_cvt_f32_i32_e32 v112, v112
	v_cvt_f32_i32_e32 v113, v113
	v_cvt_f32_i32_e32 v114, v114
	v_cvt_f32_i32_e32 v115, v115
	v_cvt_f32_i32_e32 v124, v124
	v_cvt_f32_i32_e32 v125, v125
	v_cvt_f32_i32_e32 v126, v126
	v_cvt_f32_i32_e32 v127, v127
	v_cvt_f32_i32_e32 v116, v116
	v_cvt_f32_i32_e32 v117, v117
	v_cvt_f32_i32_e32 v118, v118
	v_cvt_f32_i32_e32 v119, v119
	v_pk_mul_f32 v[64:65], v[120:121], v[78:79] op_sel_hi:[1,0]
	v_pk_mul_f32 v[66:67], v[122:123], v[78:79] op_sel_hi:[1,0]
	v_pk_mul_f32 v[68:69], v[112:113], v[78:79] op_sel_hi:[1,0]
	v_pk_mul_f32 v[70:71], v[114:115], v[78:79] op_sel_hi:[1,0]
	v_exp_f32_e32 v64, v64
	v_exp_f32_e32 v65, v65
	v_exp_f32_e32 v66, v66
	v_exp_f32_e32 v67, v67
	v_exp_f32_e32 v68, v68
	v_exp_f32_e32 v69, v69
	v_exp_f32_e32 v70, v70
	v_exp_f32_e32 v71, v71
	v_pk_mul_f32 v[120:121], v[124:125], v[120:121]
	v_pk_mul_f32 v[122:123], v[126:127], v[122:123]
	v_pk_mul_f32 v[112:113], v[116:117], v[112:113]
	v_pk_mul_f32 v[114:115], v[118:119], v[114:115]
	v_pk_fma_f32 v[64:65], v[64:65], v[20:21], v[20:21] op_sel_hi:[1,0,0]
	v_pk_fma_f32 v[66:67], v[66:67], v[20:21], v[20:21] op_sel_hi:[1,0,0]
	v_pk_fma_f32 v[68:69], v[68:69], v[20:21], v[20:21] op_sel_hi:[1,0,0]
	v_pk_fma_f32 v[70:71], v[70:71], v[20:21], v[20:21] op_sel_hi:[1,0,0]
	v_rcp_f32_e32 v64, v64
	v_rcp_f32_e32 v65, v65
	v_rcp_f32_e32 v66, v66
	v_rcp_f32_e32 v67, v67
	v_rcp_f32_e32 v68, v68
	v_rcp_f32_e32 v69, v69
	v_rcp_f32_e32 v70, v70
	v_rcp_f32_e32 v71, v71
	v_add_u32_e32 v76, 0x160000, v232
	v_pk_mul_f32 v[120:121], v[120:121], v[64:65]
	v_pk_mul_f32 v[122:123], v[122:123], v[66:67]
	v_pk_mul_f32 v[112:113], v[112:113], v[68:69]
	v_pk_mul_f32 v[114:115], v[114:115], v[70:71]
	v_cvt_pk_bf16_f32 v72, v120, v121
	v_cvt_pk_bf16_f32 v73, v122, v123
	v_cvt_pk_bf16_f32 v74, v112, v113
	v_cvt_pk_bf16_f32 v75, v114, v115
	global_store_dwordx4 v76, v[72:75], s[8:9]
	v_mul_f32_e32 v94, 0xbfb8aa3b, v229
	v_mul_f32_e32 v24, v229, v229
	v_rcp_f32_e32 v24, v24
	v_cvt_f32_i32_e32 v104, v104
	v_cvt_f32_i32_e32 v105, v105
	v_cvt_f32_i32_e32 v106, v106
	v_cvt_f32_i32_e32 v107, v107
	v_cvt_f32_i32_e32 v96, v96
	v_cvt_f32_i32_e32 v97, v97
	v_cvt_f32_i32_e32 v98, v98
	v_cvt_f32_i32_e32 v99, v99
	v_cvt_f32_i32_e32 v108, v108
	v_cvt_f32_i32_e32 v109, v109
	v_cvt_f32_i32_e32 v110, v110
	v_cvt_f32_i32_e32 v111, v111
	v_cvt_f32_i32_e32 v100, v100
	v_cvt_f32_i32_e32 v101, v101
	v_cvt_f32_i32_e32 v102, v102
	v_cvt_f32_i32_e32 v103, v103
	v_pk_mul_f32 v[80:81], v[104:105], v[94:95] op_sel_hi:[1,0]
	v_pk_mul_f32 v[82:83], v[106:107], v[94:95] op_sel_hi:[1,0]
	v_pk_mul_f32 v[84:85], v[96:97], v[94:95] op_sel_hi:[1,0]
	v_pk_mul_f32 v[86:87], v[98:99], v[94:95] op_sel_hi:[1,0]
	v_exp_f32_e32 v80, v80
	v_exp_f32_e32 v81, v81
	v_exp_f32_e32 v82, v82
	v_exp_f32_e32 v83, v83
	v_exp_f32_e32 v84, v84
	v_exp_f32_e32 v85, v85
	v_exp_f32_e32 v86, v86
	v_exp_f32_e32 v87, v87
	v_pk_mul_f32 v[104:105], v[108:109], v[104:105]
	v_pk_mul_f32 v[106:107], v[110:111], v[106:107]
	v_pk_mul_f32 v[96:97], v[100:101], v[96:97]
	v_pk_mul_f32 v[98:99], v[102:103], v[98:99]
	v_pk_fma_f32 v[80:81], v[80:81], v[24:25], v[24:25] op_sel_hi:[1,0,0]
	v_pk_fma_f32 v[82:83], v[82:83], v[24:25], v[24:25] op_sel_hi:[1,0,0]
	v_pk_fma_f32 v[84:85], v[84:85], v[24:25], v[24:25] op_sel_hi:[1,0,0]
	v_pk_fma_f32 v[86:87], v[86:87], v[24:25], v[24:25] op_sel_hi:[1,0,0]
	v_rcp_f32_e32 v80, v80
	v_rcp_f32_e32 v81, v81
	v_rcp_f32_e32 v82, v82
	v_rcp_f32_e32 v83, v83
	v_rcp_f32_e32 v84, v84
	v_rcp_f32_e32 v85, v85
	v_rcp_f32_e32 v86, v86
	v_rcp_f32_e32 v87, v87
	v_add_u32_e32 v92, 0x18c000, v232
	v_pk_mul_f32 v[104:105], v[104:105], v[80:81]
	v_pk_mul_f32 v[106:107], v[106:107], v[82:83]
	v_pk_mul_f32 v[96:97], v[96:97], v[84:85]
	v_pk_mul_f32 v[98:99], v[98:99], v[86:87]
	v_cvt_pk_bf16_f32 v88, v104, v105
	v_cvt_pk_bf16_f32 v89, v106, v107
	v_cvt_pk_bf16_f32 v90, v96, v97
	v_cvt_pk_bf16_f32 v91, v98, v99
	global_store_dwordx4 v92, v[88:91], s[8:9]
	v_mul_f32_e32 v78, 0xbfb8aa3b, v230
	v_mul_f32_e32 v20, v230, v230
	v_rcp_f32_e32 v20, v20
	v_cvt_f32_i32_e32 v48, v48
	v_cvt_f32_i32_e32 v49, v49
	v_cvt_f32_i32_e32 v50, v50
	v_cvt_f32_i32_e32 v51, v51
	v_cvt_f32_i32_e32 v16, v16
	v_cvt_f32_i32_e32 v17, v17
	v_cvt_f32_i32_e32 v18, v18
	v_cvt_f32_i32_e32 v19, v19
	v_cvt_f32_i32_e32 v60, v60
	v_cvt_f32_i32_e32 v61, v61
	v_cvt_f32_i32_e32 v62, v62
	v_cvt_f32_i32_e32 v63, v63
	v_cvt_f32_i32_e32 v44, v44
	v_cvt_f32_i32_e32 v45, v45
	v_cvt_f32_i32_e32 v46, v46
	v_cvt_f32_i32_e32 v47, v47
	v_pk_mul_f32 v[64:65], v[48:49], v[78:79] op_sel_hi:[1,0]
	v_pk_mul_f32 v[66:67], v[50:51], v[78:79] op_sel_hi:[1,0]
	v_pk_mul_f32 v[68:69], v[16:17], v[78:79] op_sel_hi:[1,0]
	v_pk_mul_f32 v[70:71], v[18:19], v[78:79] op_sel_hi:[1,0]
	v_exp_f32_e32 v64, v64
	v_exp_f32_e32 v65, v65
	v_exp_f32_e32 v66, v66
	v_exp_f32_e32 v67, v67
	v_exp_f32_e32 v68, v68
	v_exp_f32_e32 v69, v69
	v_exp_f32_e32 v70, v70
	v_exp_f32_e32 v71, v71
	v_pk_mul_f32 v[48:49], v[60:61], v[48:49]
	v_pk_mul_f32 v[50:51], v[62:63], v[50:51]
	v_pk_mul_f32 v[16:17], v[44:45], v[16:17]
	v_pk_mul_f32 v[18:19], v[46:47], v[18:19]
	v_pk_fma_f32 v[64:65], v[64:65], v[20:21], v[20:21] op_sel_hi:[1,0,0]
	v_pk_fma_f32 v[66:67], v[66:67], v[20:21], v[20:21] op_sel_hi:[1,0,0]
	v_pk_fma_f32 v[68:69], v[68:69], v[20:21], v[20:21] op_sel_hi:[1,0,0]
	v_pk_fma_f32 v[70:71], v[70:71], v[20:21], v[20:21] op_sel_hi:[1,0,0]
	v_rcp_f32_e32 v64, v64
	v_rcp_f32_e32 v65, v65
	v_rcp_f32_e32 v66, v66
	v_rcp_f32_e32 v67, v67
	v_rcp_f32_e32 v68, v68
	v_rcp_f32_e32 v69, v69
	v_rcp_f32_e32 v70, v70
	v_rcp_f32_e32 v71, v71
	v_add_u32_e32 v76, 0x1b8000, v232
	v_pk_mul_f32 v[48:49], v[48:49], v[64:65]
	v_pk_mul_f32 v[50:51], v[50:51], v[66:67]
	v_pk_mul_f32 v[16:17], v[16:17], v[68:69]
	v_pk_mul_f32 v[18:19], v[18:19], v[70:71]
	v_cvt_pk_bf16_f32 v72, v48, v49
	v_cvt_pk_bf16_f32 v73, v50, v51
	v_cvt_pk_bf16_f32 v74, v16, v17
	v_cvt_pk_bf16_f32 v75, v18, v19
	global_store_dwordx4 v76, v[72:75], s[8:9]
	v_mul_f32_e32 v94, 0xbfb8aa3b, v231
	v_mul_f32_e32 v24, v231, v231
	v_rcp_f32_e32 v24, v24
	v_cvt_f32_i32_e32 v8, v8
	v_cvt_f32_i32_e32 v9, v9
	v_cvt_f32_i32_e32 v10, v10
	v_cvt_f32_i32_e32 v11, v11
	v_cvt_f32_i32_e32 v0, v0
	v_cvt_f32_i32_e32 v1, v1
	v_cvt_f32_i32_e32 v2, v2
	v_cvt_f32_i32_e32 v3, v3
	v_cvt_f32_i32_e32 v12, v12
	v_cvt_f32_i32_e32 v13, v13
	v_cvt_f32_i32_e32 v14, v14
	v_cvt_f32_i32_e32 v15, v15
	v_cvt_f32_i32_e32 v4, v4
	v_cvt_f32_i32_e32 v5, v5
	v_cvt_f32_i32_e32 v6, v6
	v_cvt_f32_i32_e32 v7, v7
	v_pk_mul_f32 v[80:81], v[8:9], v[94:95] op_sel_hi:[1,0]
	v_pk_mul_f32 v[82:83], v[10:11], v[94:95] op_sel_hi:[1,0]
	v_pk_mul_f32 v[84:85], v[0:1], v[94:95] op_sel_hi:[1,0]
	v_pk_mul_f32 v[86:87], v[2:3], v[94:95] op_sel_hi:[1,0]
	v_exp_f32_e32 v80, v80
	v_exp_f32_e32 v81, v81
	v_exp_f32_e32 v82, v82
	v_exp_f32_e32 v83, v83
	v_exp_f32_e32 v84, v84
	v_exp_f32_e32 v85, v85
	v_exp_f32_e32 v86, v86
	v_exp_f32_e32 v87, v87
	v_pk_mul_f32 v[8:9], v[12:13], v[8:9]
	v_pk_mul_f32 v[10:11], v[14:15], v[10:11]
	v_pk_mul_f32 v[0:1], v[4:5], v[0:1]
	v_pk_mul_f32 v[2:3], v[6:7], v[2:3]
	v_pk_fma_f32 v[80:81], v[80:81], v[24:25], v[24:25] op_sel_hi:[1,0,0]
	v_pk_fma_f32 v[82:83], v[82:83], v[24:25], v[24:25] op_sel_hi:[1,0,0]
	v_pk_fma_f32 v[84:85], v[84:85], v[24:25], v[24:25] op_sel_hi:[1,0,0]
	v_pk_fma_f32 v[86:87], v[86:87], v[24:25], v[24:25] op_sel_hi:[1,0,0]
	v_rcp_f32_e32 v80, v80
	v_rcp_f32_e32 v81, v81
	v_rcp_f32_e32 v82, v82
	v_rcp_f32_e32 v83, v83
	v_rcp_f32_e32 v84, v84
	v_rcp_f32_e32 v85, v85
	v_rcp_f32_e32 v86, v86
	v_rcp_f32_e32 v87, v87
	v_add_u32_e32 v92, 0x1e4000, v232
	v_pk_mul_f32 v[8:9], v[8:9], v[80:81]
	v_pk_mul_f32 v[10:11], v[10:11], v[82:83]
	v_pk_mul_f32 v[0:1], v[0:1], v[84:85]
	v_pk_mul_f32 v[2:3], v[2:3], v[86:87]
	v_cvt_pk_bf16_f32 v88, v8, v9
	v_cvt_pk_bf16_f32 v89, v10, v11
	v_cvt_pk_bf16_f32 v90, v0, v1
	v_cvt_pk_bf16_f32 v91, v2, v3
	global_store_dwordx4 v92, v[88:91], s[8:9]
	s_andn2_b64 vcc, exec, s[4:5]
	s_mov_b64 s[4:5], -1
	s_cbranch_vccnz .LBB0_749
	s_andn2_b64 vcc, exec, s[6:7]
	s_cbranch_vccnz .LBB0_748
	s_barrier
	s_branch .LBB0_748
